# split grid barrier 8 by role: scan blocks wait at seam, conversion blocks wait after their conversions, meta-row projection blocks wait before the row-scale load
# baseline (speedup 1.0000x reference)
.Lgb_chk_8:
	v_mov_b32_e32 v11, s89
	v_cmp_lt_u32_e32 vcc, 0xdf, v11
	s_cbranch_vccz .Lgb_done_8

.LBB0_1443:
	s_cmp_lt_i32 s89, 32
	s_cbranch_scc1 .Lgw_end_8a
	s_cmpk_gt_i32 s89, 0xdf
	s_cbranch_scc1 .Lgw_end_8a
	s_cmp_lg_u32 s92, 0
	s_cbranch_scc1 .Lgw_end_8a
	v_mov_b32_e32 v68, 0x22160
	ds_read_b32 v69, v68
	v_mov_b32_e32 v70, s99
	v_lshrrev_b32_e32 v71, 16, v70
	v_mov_b32_e32 v72, s98
	v_min_u32_e32 v72, 8, v72
	v_mov_b32_e32 v73, 0
	s_waitcnt lgkmcnt(0)
	v_mul_lo_u32 v72, v72, v69
.Lgw_poll_8a:
	global_load_dword v74, v71, s[100:101] sc1
	v_add_u32_e32 v73, 1, v73
	s_waitcnt vmcnt(0)
	v_cmp_ge_u32_e32 vcc, v74, v72
	s_cbranch_vccnz .Lgw_end_8a
	v_cmp_gt_u32_e32 vcc, 0x80000, v73
	s_sleep 1
	s_cbranch_vccnz .Lgw_poll_8a

.LBB0_1449:
	v_add_u32_e32 v14, s14, v222
	v_ashrrev_i32_e32 v15, 31, v14
	v_lshlrev_b64 v[14:15], 11, v[14:15]
	v_lshl_add_u64 v[60:61], v[6:7], 0, v[14:15]
	v_add_co_u32_e32 v62, vcc, 0x8000, v60
	global_load_dwordx4 v[14:17], v[60:61], off
	global_load_dwordx4 v[18:21], v[4:5], off
	v_addc_co_u32_e32 v63, vcc, 0, v61, vcc
	v_add_co_u32_e32 v64, vcc, 0x10000, v60
	global_load_dwordx4 v[22:25], v[62:63], off
	s_nop 0
	v_addc_co_u32_e32 v65, vcc, 0, v61, vcc
	v_add_co_u32_e32 v66, vcc, 0x18000, v60
	global_load_dwordx4 v[26:29], v[64:65], off
	s_nop 0
	v_addc_co_u32_e32 v67, vcc, 0, v61, vcc
	global_load_dwordx4 v[30:33], v[66:67], off
	global_load_dwordx4 v[36:39], v[60:61], off offset:64
	global_load_dwordx4 v[40:43], v[4:5], off offset:64
	global_load_dwordx4 v[44:47], v[62:63], off offset:64
	global_load_dwordx4 v[48:51], v[64:65], off offset:64
	global_load_dwordx4 v[52:55], v[66:67], off offset:64
	s_and_b64 vcc, exec, s[4:5]
	s_waitcnt vmcnt(0)
	v_mfma_f32_16x16x32_bf16 v[14:17], v[14:17], v[18:21], 0
	v_mfma_f32_16x16x32_bf16 v[22:25], v[22:25], v[18:21], 0
	v_mfma_f32_16x16x32_bf16 v[26:29], v[26:29], v[18:21], 0
	v_mfma_f32_16x16x32_bf16 v[18:21], v[30:33], v[18:21], 0
	global_load_dwordx4 v[30:33], v[60:61], off offset:128
	global_load_dwordx4 v[56:59], v[4:5], off offset:128
	v_mfma_f32_16x16x32_bf16 v[14:17], v[36:39], v[40:43], v[14:17]
	global_load_dwordx4 v[36:39], v[62:63], off offset:128
	v_mfma_f32_16x16x32_bf16 v[22:25], v[44:47], v[40:43], v[22:25]
	global_load_dwordx4 v[44:47], v[64:65], off offset:128
	v_mfma_f32_16x16x32_bf16 v[26:29], v[48:51], v[40:43], v[26:29]
	global_load_dwordx4 v[48:51], v[66:67], off offset:128
	v_mfma_f32_16x16x32_bf16 v[18:21], v[52:55], v[40:43], v[18:21]
	global_load_dwordx4 v[40:43], v[60:61], off offset:192
	global_load_dwordx4 v[52:55], v[4:5], off offset:192
	s_waitcnt vmcnt(0)
	v_mfma_f32_16x16x32_bf16 v[14:17], v[30:33], v[56:59], v[14:17]
	global_load_dwordx4 v[30:33], v[62:63], off offset:192
	v_mfma_f32_16x16x32_bf16 v[22:25], v[36:39], v[56:59], v[22:25]
	global_load_dwordx4 v[36:39], v[64:65], off offset:192
	v_mfma_f32_16x16x32_bf16 v[26:29], v[44:47], v[56:59], v[26:29]
	global_load_dwordx4 v[44:47], v[66:67], off offset:192
	s_waitcnt lgkmcnt(0)
	s_barrier
	v_mfma_f32_16x16x32_bf16 v[18:21], v[48:51], v[56:59], v[18:21]
	v_mfma_f32_16x16x32_bf16 v[14:17], v[40:43], v[52:55], v[14:17]
	s_waitcnt vmcnt(2)
	v_mfma_f32_16x16x32_bf16 v[22:25], v[30:33], v[52:55], v[22:25]
	s_waitcnt vmcnt(1)
	v_mfma_f32_16x16x32_bf16 v[26:29], v[36:39], v[52:55], v[26:29]
	s_waitcnt vmcnt(0)
	v_mfma_f32_16x16x32_bf16 v[18:21], v[44:47], v[52:55], v[18:21]
	s_nop 1
	ds_write_b128 v34, v[14:17]
	s_nop 0
	ds_write_b128 v34, v[22:25] offset:1024
	s_nop 0
	ds_write_b128 v34, v[26:29] offset:2048
	s_nop 0
	ds_write_b128 v34, v[18:21] offset:3072
	s_waitcnt lgkmcnt(0)
	s_barrier
	s_cbranch_vccnz .LBB0_1448
	ds_read_b128 v[14:17], v1
	ds_read_b128 v[18:21], v1 offset:4096
	ds_read_b128 v[22:25], v1 offset:8192
	ds_read_b128 v[36:39], v1 offset:1024
	ds_read_b128 v[40:43], v1 offset:5120
	s_cmp_lt_i32 s19, 16
	s_waitcnt lgkmcnt(3)
	v_pk_add_f32 v[14:15], v[14:15], v[18:19]
	v_pk_add_f32 v[20:21], v[16:17], v[20:21]
	s_waitcnt lgkmcnt(2)
	v_pk_add_f32 v[30:31], v[14:15], v[22:23]
	v_mov_b32_e32 v68, 0x22160
	ds_read_b32 v69, v68
	v_mov_b32_e32 v70, s99
	v_lshrrev_b32_e32 v71, 16, v70
	v_mov_b32_e32 v72, s98
	v_min_u32_e32 v72, 8, v72
	v_mov_b32_e32 v73, 0
	s_waitcnt lgkmcnt(0)
	v_mul_lo_u32 v72, v72, v69

.Lgw_end_8b:
	global_load_dword v14, v[8:9], off
	ds_read_b128 v[16:19], v1 offset:9216
	v_pk_add_f32 v[28:29], v[20:21], v[24:25]
	ds_read_b128 v[24:27], v1 offset:12288
	ds_read_b128 v[20:23], v1 offset:16384
	ds_read_b128 v[44:47], v1 offset:13312
	s_cselect_b64 s[10:11], -1, 0
	s_cmp_gt_i32 s19, 15
	s_waitcnt lgkmcnt(2)
	v_pk_add_f32 v[28:29], v[28:29], v[26:27]
	v_pk_add_f32 v[30:31], v[30:31], v[24:25]
	ds_read_b128 v[24:27], v1 offset:20480
	ds_read_b128 v[48:51], v1 offset:17408
	s_waitcnt lgkmcnt(3)
	v_pk_add_f32 v[28:29], v[28:29], v[22:23]
	v_pk_add_f32 v[30:31], v[30:31], v[20:21]
	ds_read_b128 v[20:23], v1 offset:24576
	ds_read_b128 v[52:55], v1 offset:21504
	s_waitcnt lgkmcnt(3)
	v_pk_add_f32 v[28:29], v[28:29], v[26:27]
	v_pk_add_f32 v[30:31], v[30:31], v[24:25]
	ds_read_b128 v[24:27], v1 offset:28672
	ds_read_b128 v[56:59], v1 offset:25600
	s_waitcnt lgkmcnt(3)
	v_pk_add_f32 v[28:29], v[28:29], v[22:23]
	v_pk_add_f32 v[32:33], v[30:31], v[20:21]
	ds_read_b128 v[20:23], v1 offset:29696
	s_waitcnt lgkmcnt(2)
	v_pk_add_f32 v[30:31], v[28:29], v[26:27]
	v_pk_add_f32 v[28:29], v[32:33], v[24:25]
	v_pk_add_f32 v[24:25], v[38:39], v[42:43]
	v_pk_add_f32 v[26:27], v[36:37], v[40:41]
	v_pk_add_f32 v[18:19], v[24:25], v[18:19]
	v_pk_add_f32 v[16:17], v[26:27], v[16:17]
	v_pk_add_f32 v[18:19], v[18:19], v[46:47]
	v_pk_add_f32 v[16:17], v[16:17], v[44:45]
	v_pk_add_f32 v[18:19], v[18:19], v[50:51]
	v_pk_add_f32 v[16:17], v[16:17], v[48:49]
	v_pk_add_f32 v[18:19], v[18:19], v[54:55]
	v_pk_add_f32 v[16:17], v[16:17], v[52:53]
	s_waitcnt lgkmcnt(1)
	v_pk_add_f32 v[18:19], v[18:19], v[58:59]
	v_pk_add_f32 v[24:25], v[16:17], v[56:57]
	s_waitcnt lgkmcnt(0)
	v_pk_add_f32 v[26:27], v[18:19], v[22:23]
	ds_read_b128 v[16:19], v1 offset:2048
	ds_read_b128 v[36:39], v1 offset:6144
	v_pk_add_f32 v[24:25], v[24:25], v[20:21]
	ds_read_b128 v[20:23], v1 offset:10240
	ds_read_b128 v[40:43], v1 offset:3072
	ds_read_b128 v[44:47], v1 offset:7168
	s_waitcnt lgkmcnt(3)
	v_pk_add_f32 v[32:33], v[18:19], v[38:39]
	v_pk_add_f32 v[48:49], v[16:17], v[36:37]
	ds_read_b128 v[16:19], v1 offset:14336
	ds_read_b128 v[36:39], v1 offset:11264
	s_waitcnt lgkmcnt(4)
	v_pk_add_f32 v[32:33], v[32:33], v[22:23]
	v_pk_add_f32 v[52:53], v[48:49], v[20:21]
	ds_read_b128 v[20:23], v1 offset:18432
	ds_read_b128 v[48:51], v1 offset:15360
	s_waitcnt lgkmcnt(3)
	v_pk_add_f32 v[32:33], v[32:33], v[18:19]
	v_pk_add_f32 v[56:57], v[52:53], v[16:17]
	ds_read_b128 v[16:19], v1 offset:22528
	ds_read_b128 v[52:55], v1 offset:19456
	s_waitcnt lgkmcnt(3)
	v_pk_add_f32 v[32:33], v[32:33], v[22:23]
	v_pk_add_f32 v[60:61], v[56:57], v[20:21]
	ds_read_b128 v[20:23], v1 offset:26624
	ds_read_b128 v[56:59], v1 offset:23552
	s_waitcnt lgkmcnt(3)
	v_pk_add_f32 v[32:33], v[32:33], v[18:19]
	v_pk_add_f32 v[64:65], v[60:61], v[16:17]
	ds_read_b128 v[16:19], v1 offset:30720
	ds_read_b128 v[60:63], v1 offset:27648
	s_waitcnt lgkmcnt(3)
	v_pk_add_f32 v[22:23], v[32:33], v[22:23]
	v_pk_add_f32 v[20:21], v[64:65], v[20:21]
	ds_read_b128 v[64:67], v1 offset:31744
	s_waitcnt lgkmcnt(2)
	v_pk_add_f32 v[22:23], v[22:23], v[18:19]
	v_pk_add_f32 v[20:21], v[20:21], v[16:17]
	v_pk_add_f32 v[16:17], v[42:43], v[46:47]
	v_pk_add_f32 v[18:19], v[40:41], v[44:45]
	v_pk_add_f32 v[16:17], v[16:17], v[38:39]
	v_pk_add_f32 v[18:19], v[18:19], v[36:37]
	v_pk_add_f32 v[16:17], v[16:17], v[50:51]
	v_pk_add_f32 v[18:19], v[18:19], v[48:49]
	v_pk_add_f32 v[16:17], v[16:17], v[54:55]
	v_pk_add_f32 v[18:19], v[18:19], v[52:53]
	v_pk_add_f32 v[16:17], v[16:17], v[58:59]
	v_pk_add_f32 v[18:19], v[18:19], v[56:57]
	s_waitcnt lgkmcnt(1)
	v_pk_add_f32 v[16:17], v[16:17], v[62:63]
	v_pk_add_f32 v[32:33], v[18:19], v[60:61]
	s_waitcnt lgkmcnt(0)
	v_pk_add_f32 v[18:19], v[16:17], v[66:67]
	v_pk_add_f32 v[16:17], v[32:33], v[64:65]
	s_cbranch_scc1 .LBB0_1452
	v_pk_mul_f32 v[32:33], v[30:31], v[30:31]
	v_pk_mul_f32 v[36:37], v[28:29], v[28:29]
	v_mul_f32_e32 v13, v16, v16
	v_pk_mov_b32 v[38:39], v[36:37], v[32:33] op_sel:[1,0]
	v_mov_b32_e32 v37, v33
	v_pk_add_f32 v[32:33], v[38:39], v[36:37]
	v_pk_mul_f32 v[36:37], v[26:27], v[26:27]
	v_pk_mul_f32 v[38:39], v[24:25], v[24:25]
	v_mul_f32_e32 v15, v17, v17
	v_pk_mov_b32 v[40:41], v[38:39], v[36:37] op_sel:[1,0]
	v_mov_b32_e32 v39, v37
	v_pk_add_f32 v[36:37], v[40:41], v[38:39]
	v_pk_add_f32 v[32:33], v[32:33], v[32:33] op_sel:[0,1] op_sel_hi:[1,0]
	v_pk_add_f32 v[36:37], v[36:37], v[36:37] op_sel:[0,1] op_sel_hi:[1,0]
	v_mov_b32_e32 v33, v13
	v_mov_b32_e32 v37, v15
	v_pk_add_f32 v[32:33], v[32:33], v[36:37]
	v_mul_f32_e32 v36, v21, v21
	v_mul_f32_e32 v38, v18, v18
	v_pk_fma_f32 v[36:37], v[20:21], v[20:21], v[36:37] op_sel_hi:[1,1,0]
	v_mul_f32_e32 v40, v19, v19
	v_mov_b32_e32 v37, v38
	v_mul_f32_e32 v38, v23, v23
	v_pk_fma_f32 v[38:39], v[22:23], v[22:23], v[38:39] op_sel_hi:[1,1,0]
	v_xor_b32_e32 v15, 16, v35
	v_mov_b32_e32 v39, v40
	v_pk_add_f32 v[36:37], v[36:37], v[38:39]
	s_nop 0
	v_pk_add_f32 v[32:33], v[32:33], v[36:37]
	s_nop 0
	v_add_f32_e32 v13, v32, v33
	v_and_b32_e32 v32, 64, v35
	v_add_u32_e32 v32, 64, v32
	v_cmp_lt_i32_e32 vcc, v15, v32
	s_nop 1
	v_cndmask_b32_e32 v15, v35, v15, vcc
	v_lshlrev_b32_e32 v15, 2, v15
	ds_bpermute_b32 v15, v15, v13
	s_waitcnt lgkmcnt(0)
	v_add_f32_e32 v13, v13, v15
	v_xor_b32_e32 v15, 32, v35
	v_cmp_lt_i32_e32 vcc, v15, v32
	s_nop 1
	v_cndmask_b32_e32 v15, v35, v15, vcc
	v_lshlrev_b32_e32 v15, 2, v15
	ds_bpermute_b32 v15, v15, v13
	s_waitcnt lgkmcnt(0)
	v_add_f32_e32 v13, v13, v15
	s_waitcnt vmcnt(0)
	v_mul_f32_e32 v15, v14, v14
	v_mul_f32_e32 v15, 0x3c800000, v15
	v_fmaak_f32 v13, v15, v13, 0x358637bd
	v_mul_f32_e32 v15, 0x4b800000, v13
	v_cmp_gt_f32_e32 vcc, s16, v13
	s_nop 1
	v_cndmask_b32_e32 v13, v13, v15, vcc
	v_rsq_f32_e32 v13, v13
	s_nop 0
	v_mul_f32_e32 v15, 0x45800000, v13
	v_cndmask_b32_e32 v13, v13, v15, vcc
	v_mul_f32_e32 v14, v14, v13
